# conversion unit: counted vmcnt waits (strip 0 only before packing; counted wait before first strip-1 use) on top of previous edits
# speedup vs baseline: 1.0049x; 1.0049x over previous
; #define GAS __attribute__((address_space(1)))
; __device__ __forceinline__ void tr_load(const TrBlk& t, int wave, int lane, f32x4 (&v)[16]) {
; #pragma unroll
;     for (int i = 0; i < 16; ++i) v[i] = __builtin_nontemporal_load((const f32x4 GAS*)((const char GAS*)t.src + (size_t)(16 * wave + i) * t.N * 4 + 16u * lane));
; template <int NBK> __device__ __forceinline__ void tr_blocks(Ctx& C, int L, int b0) {
;     ...
;     const TrBlk t0 = tr_decode(C, L, b0), t1 = tr_decode(C, L, b0 + (NBK > 1 ? 1 : 0)), t2 = tr_decode(C, L, b0 + (NBK > 2 ? 2 : 0)), t3 = tr_decode(C, L, b0 + (NBK > 3 ? 3 : 0));
;     tr_load(t0, C.wave, C.lane, r0); if (NBK > 1) tr_load(t1, C.wave, C.lane, r1); if (NBK > 2) tr_load(t2, C.wave, C.lane, r2);
.LBB0_997:
	s_ashr_i32 s24, s74, 6
	s_add_u32 s10, s10, s58
	s_addc_u32 s11, s11, s59
	s_and_b64 s[58:59], s[6:7], exec
	s_cselect_b32 s19, s82, 0x1b200000
	s_and_b64 s[54:55], s[54:55], exec
	s_cselect_b32 s19, 0x2200000, s19
	s_and_b64 s[54:55], s[56:57], exec
	s_cselect_b32 s19, 0x400000, s19
	s_add_u32 s58, s50, s19
	s_addc_u32 s59, s51, 0
	s_cmp_eq_u32 s18, 2
	s_cselect_b64 s[54:55], -1, 0
	s_and_b64 s[54:55], s[12:13], s[54:55]
	s_and_b64 s[54:55], s[54:55], exec
	s_cselect_b32 s19, s81, 0x800
	s_and_b64 s[54:55], s[12:13], exec
	s_cselect_b32 s54, s97, 0
	s_mul_i32 s60, s19, s54
	s_mul_hi_i32 s61, s19, s54
	s_and_b64 s[54:55], s[6:7], exec
	s_cselect_b32 s62, 0x600, s78
	s_and_b64 s[54:55], s[56:57], exec
	s_cselect_b32 s54, 0xf00, s62
	s_mul_i32 s55, s61, s54
	s_mul_hi_u32 s56, s60, s54
	s_add_i32 s56, s56, s55
	s_mul_i32 s54, s60, s54
	s_add_u32 s54, s58, s54
	s_mul_i32 s96, s96, 48
	s_addc_u32 s55, s59, s56
	s_sub_i32 s56, s95, s96
	s_and_b64 s[12:13], s[12:13], exec
	s_cselect_b32 s56, s56, s94
	s_abs_i32 s57, s93
	v_cvt_f32_u32_e32 v2, s57
	s_sub_i32 s58, 0, s57
	s_abs_i32 s13, s56
	s_xor_b32 s12, s56, s93
	v_rcp_iflag_f32_e32 v2, v2
	s_ashr_i32 s12, s12, 31
	s_load_dwordx2 s[10:11], s[10:11], 0x0
	s_mul_i32 s61, s61, s35
	v_mul_f32_e32 v2, 0x4f7ffffe, v2
	v_cvt_u32_f32_e32 v2, v2
	s_mul_i32 s91, s91, 48
	v_and_b32_e32 v133, 63, v131
	v_lshlrev_b32_e32 v132, 4, v133
	v_readfirstlane_b32 s59, v2
	s_mul_i32 s58, s58, s59
	s_mul_hi_u32 s58, s59, s58
	s_add_i32 s59, s59, s58
	s_mul_hi_u32 s58, s13, s59
	s_mul_i32 s59, s58, s57
	s_sub_i32 s13, s13, s59
	s_add_i32 s59, s58, 1
	s_sub_i32 s62, s13, s57
	s_cmp_ge_u32 s13, s57
	s_cselect_b32 s58, s59, s58
	s_cselect_b32 s13, s62, s13
	s_add_i32 s59, s58, 1
	s_cmp_ge_u32 s13, s57
	s_cselect_b32 s13, s59, s58
	s_xor_b32 s13, s13, s12
	s_sub_i32 s57, s13, s12
	s_lshl_b32 s58, s57, 7
	s_ashr_i32 s13, s58, 31
	s_add_u32 s12, s54, s58
	s_mul_hi_u32 s54, s60, s35
	s_addc_u32 s13, s55, s13
	s_add_i32 s55, s54, s61
	s_mul_i32 s54, s60, s35
	s_lshl_b64 s[54:55], s[54:55], 2
	s_waitcnt lgkmcnt(0)
	s_add_u32 s54, s10, s54
	s_addc_u32 s55, s11, s55
	s_mul_hi_i32 s11, s58, s35
	s_mul_i32 s10, s58, s35
	s_lshl_b64 s[10:11], s[10:11], 2
	s_add_u32 s58, s54, s10
	s_mul_i32 s57, s57, s93
	s_addc_u32 s59, s55, s11
	s_sub_i32 s10, s56, s57
	s_lshl_b32 s10, s10, 8
	s_ashr_i32 s11, s10, 31
	s_lshl_b64 s[54:55], s[10:11], 2
	s_add_u32 s54, s58, s54
	s_addc_u32 s55, s59, s55
	s_and_b64 s[56:57], s[8:9], exec
	s_cselect_b32 s11, s82, 0x1b200000
	s_and_b64 s[46:47], s[46:47], exec
	s_cselect_b32 s11, 0x2200000, s11
	s_and_b64 s[46:47], s[48:49], exec
	s_cselect_b32 s11, 0x400000, s11
	s_add_u32 s50, s50, s11
	s_addc_u32 s51, s51, 0
	s_cmp_eq_u32 s34, 2
	s_cselect_b64 s[46:47], -1, 0
	s_and_b64 s[46:47], s[44:45], s[46:47]
	s_and_b64 s[46:47], s[46:47], exec
	s_cselect_b32 s11, s81, 0x800
	s_and_b64 s[46:47], s[44:45], exec
	s_cselect_b32 s46, s92, 0
	s_mul_i32 s56, s11, s46
	s_mul_hi_i32 s57, s11, s46
	s_and_b64 s[46:47], s[8:9], exec
	s_cselect_b32 s58, 0x600, s78
	s_and_b64 s[46:47], s[48:49], exec
	s_cselect_b32 s46, 0xf00, s58
	s_mul_i32 s47, s57, s46
	s_mul_hi_u32 s48, s56, s46
	s_add_i32 s48, s48, s47
	s_mul_i32 s46, s56, s46
	s_add_u32 s46, s50, s46
	s_addc_u32 s47, s51, s48
	s_sub_i32 s48, s90, s91
	s_and_b64 s[44:45], s[44:45], exec
	s_cselect_b32 s48, s48, s89
	s_abs_i32 s49, s88
	v_cvt_f32_u32_e32 v2, s49
	s_sub_i32 s50, 0, s49
	s_abs_i32 s45, s48
	s_xor_b32 s44, s48, s88
	v_rcp_iflag_f32_e32 v2, v2
	s_ashr_i32 s44, s44, 31
	s_mul_i32 s57, s57, s43
	v_mov_b32_e32 v134, 0
	v_mul_f32_e32 v2, 0x4f7ffffe, v2
	v_cvt_u32_f32_e32 v2, v2
	v_mov_b32_e32 v135, 0
	v_mov_b32_e32 v136, 0
	v_mov_b32_e32 v137, 0
	v_readfirstlane_b32 s51, v2
	s_mul_i32 s50, s50, s51
	s_mul_hi_u32 s50, s51, s50
	s_add_i32 s51, s51, s50
	s_mul_hi_u32 s50, s45, s51
	s_mul_i32 s51, s50, s49
	s_sub_i32 s45, s45, s51
	s_add_i32 s51, s50, 1
	s_sub_i32 s58, s45, s49
	s_cmp_ge_u32 s45, s49
	s_cselect_b32 s50, s51, s50
	s_cselect_b32 s45, s58, s45
	s_add_i32 s51, s50, 1
	s_cmp_ge_u32 s45, s49
	s_cselect_b32 s45, s51, s50
	s_xor_b32 s45, s45, s44
	s_sub_i32 s49, s45, s44
	s_lshl_b32 s50, s49, 7
	s_ashr_i32 s44, s50, 31
	s_add_u32 s46, s46, s50
	s_addc_u32 s47, s47, s44
	s_mul_hi_u32 s44, s56, s43
	s_add_i32 s45, s44, s57
	s_mul_i32 s44, s56, s43
	s_lshl_b64 s[44:45], s[44:45], 2
	s_add_u32 s51, s52, s44
	s_addc_u32 s52, s53, s45
	s_mul_hi_i32 s45, s50, s43
	s_mul_i32 s44, s50, s43
	s_lshl_b64 s[44:45], s[44:45], 2
	s_add_u32 s50, s51, s44
	s_mul_i32 s49, s49, s88
	s_addc_u32 s51, s52, s45
	s_sub_i32 s44, s48, s49
	s_lshl_b32 s44, s44, 8
	s_ashr_i32 s45, s44, 31
	s_lshl_b64 s[48:49], s[44:45], 2
	s_add_u32 s50, s50, s48
	s_addc_u32 s51, s51, s49
	s_and_b32 s52, s74, 0xffffffc0
	s_lshl_b32 s45, s24, 4
	s_mul_i32 s48, s52, s43
	s_mul_hi_i32 s49, s52, s43
	s_add_u32 s48, s50, s48
	s_addc_u32 s49, s51, s49
	s_or_b32 s53, s52, 4
	global_load_dwordx4 v[66:69], v132, s[48:49] nt
	s_mul_i32 s48, s53, s43
	s_mul_hi_i32 s49, s53, s43
	s_add_u32 s48, s50, s48
	s_addc_u32 s49, s51, s49
	s_or_b32 s56, s52, 8
	global_load_dwordx4 v[70:73], v132, s[48:49] nt
	s_mul_i32 s48, s56, s43
	s_mul_hi_i32 s49, s56, s43
	s_add_u32 s48, s50, s48
	s_addc_u32 s49, s51, s49
	s_or_b32 s57, s52, 12
	global_load_dwordx4 v[74:77], v132, s[48:49] nt
	s_mul_i32 s48, s57, s43
	s_mul_hi_i32 s49, s57, s43
	s_add_u32 s48, s50, s48
	s_addc_u32 s49, s51, s49
	s_or_b32 s58, s52, 16
	global_load_dwordx4 v[82:85], v132, s[48:49] nt
	s_mul_i32 s48, s58, s43
	s_mul_hi_i32 s49, s58, s43
	s_add_u32 s48, s50, s48
	s_addc_u32 s49, s51, s49
	s_or_b32 s59, s52, 20
	global_load_dwordx4 v[78:81], v132, s[48:49] nt
; #define LAS __attribute__((address_space(3)))
; #define GAS __attribute__((address_space(1)))
; __device__ __forceinline__ unsigned pk4_fp8(float a, float b, float c, float d) { int p = 0; p = __builtin_amdgcn_cvt_pk_fp8_f32(a, b, p, false); p = __builtin_amdgcn_cvt_pk_fp8_f32(c, d, p, true); return (unsigned)p; }
; #define WG_BAR() do { LDS_WAIT(); __builtin_amdgcn_s_barrier(); asm volatile("" ::: "memory"); } while (0)
; __device__ __forceinline__ void tr_load(const TrBlk& t, int wave, int lane, f32x4 (&v)[16]) {
; #pragma unroll
;     for (int i = 0; i < 16; ++i) v[i] = __builtin_nontemporal_load((const f32x4 GAS*)((const char GAS*)t.src + (size_t)(16 * wave + i) * t.N * 4 + 16u * lane));
; }
; __device__ __forceinline__ void tr_pack(LAS unsigned char* buf, int wave, int lane, const f32x4 (&v)[16]) {
; #pragma unroll
;     for (int j = 0; j < 4; ++j) { u32x4 o;
; #pragma unroll
;         for (int w = 0; w < 4; ++w) o[w] = pk4_fp8(64.f * v[4 * w][j], 64.f * v[4 * w + 1][j], 64.f * v[4 * w + 2][j], 64.f * v[4 * w + 3][j]);
;         *(LAS u32x4*)(buf + (4 * lane + j) * TRP + 16 * wave) = o; }
; template <int NBK> __device__ __forceinline__ void tr_blocks(Ctx& C, int L, int b0) {
;     ...
;     tr_load(t0, C.wave, C.lane, r0); if (NBK > 1) tr_load(t1, C.wave, C.lane, r1); if (NBK > 2) tr_load(t2, C.wave, C.lane, r2);
;     WG_BAR();
;     tr_pack(buf0, C.wave, C.lane, r0);
	s_mul_i32 s48, s59, s43
	s_mul_hi_i32 s49, s59, s43
	s_add_u32 s48, s50, s48
	s_addc_u32 s49, s51, s49
	s_or_b32 s60, s52, 24
	global_load_dwordx4 v[86:89], v132, s[48:49] nt
	s_mul_i32 s48, s60, s43
	s_mul_hi_i32 s49, s60, s43
	s_add_u32 s48, s50, s48
	s_addc_u32 s49, s51, s49
	s_or_b32 s61, s52, 28
	global_load_dwordx4 v[94:97], v132, s[48:49] nt
	s_mul_i32 s48, s61, s43
	s_mul_hi_i32 s49, s61, s43
	s_add_u32 s48, s50, s48
	s_addc_u32 s49, s51, s49
	s_or_b32 s62, s52, 32
	global_load_dwordx4 v[102:105], v132, s[48:49] nt
	s_mul_i32 s48, s62, s43
	s_mul_hi_i32 s49, s62, s43
	s_add_u32 s48, s50, s48
	s_addc_u32 s49, s51, s49
	s_or_b32 s63, s52, 36
	global_load_dwordx4 v[90:93], v132, s[48:49] nt
	s_mul_i32 s48, s63, s43
	s_mul_hi_i32 s49, s63, s43
	s_add_u32 s48, s50, s48
	s_addc_u32 s49, s51, s49
	s_or_b32 s74, s52, 40
	global_load_dwordx4 v[98:101], v132, s[48:49] nt
	s_mul_i32 s48, s74, s43
	s_mul_hi_i32 s49, s74, s43
	s_add_u32 s48, s50, s48
	s_addc_u32 s49, s51, s49
	s_or_b32 s88, s52, 44
	global_load_dwordx4 v[106:109], v132, s[48:49] nt
	s_mul_i32 s48, s88, s43
	s_mul_hi_i32 s49, s88, s43
	s_add_u32 s48, s50, s48
	s_addc_u32 s49, s51, s49
	s_or_b32 s89, s52, 48
	global_load_dwordx4 v[114:117], v132, s[48:49] nt
	s_mul_i32 s48, s89, s43
	s_mul_hi_i32 s49, s89, s43
	s_add_u32 s48, s50, s48
	s_addc_u32 s49, s51, s49
	s_or_b32 s90, s52, 52
	global_load_dwordx4 v[110:113], v132, s[48:49] nt
	s_mul_i32 s48, s90, s43
	s_mul_hi_i32 s49, s90, s43
	s_add_u32 s48, s50, s48
	s_addc_u32 s49, s51, s49
	s_or_b32 s91, s52, 56
	global_load_dwordx4 v[118:121], v132, s[48:49] nt
	s_mul_i32 s48, s91, s43
	s_mul_hi_i32 s49, s91, s43
	s_add_u32 s48, s50, s48
	s_addc_u32 s49, s51, s49
	s_or_b32 s92, s52, 60
	global_load_dwordx4 v[122:125], v132, s[48:49] nt
	s_mul_hi_i32 s49, s92, s43
	s_mul_i32 s43, s92, s43
	s_add_u32 s48, s50, s43
	s_addc_u32 s49, s51, s49
	global_load_dwordx4 v[126:129], v132, s[48:49] nt
	s_mul_hi_i32 s43, s52, s35
	s_mul_i32 s52, s52, s35
	s_add_u32 s48, s54, s52
	s_addc_u32 s49, s55, s43
	s_mul_hi_i32 s43, s53, s35
	s_mul_i32 s53, s53, s35
	global_load_dwordx4 v[2:5], v132, s[48:49] nt
	s_add_u32 s48, s54, s53
	s_addc_u32 s49, s55, s43
	s_mul_hi_i32 s43, s56, s35
	s_mul_i32 s56, s56, s35
	global_load_dwordx4 v[6:9], v132, s[48:49] nt
	s_add_u32 s48, s54, s56
	s_addc_u32 s49, s55, s43
	s_mul_hi_i32 s43, s57, s35
	s_mul_i32 s57, s57, s35
	global_load_dwordx4 v[10:13], v132, s[48:49] nt
	s_add_u32 s48, s54, s57
	s_addc_u32 s49, s55, s43
	s_mul_hi_i32 s43, s58, s35
	s_mul_i32 s58, s58, s35
	global_load_dwordx4 v[18:21], v132, s[48:49] nt
	s_add_u32 s48, s54, s58
	s_addc_u32 s49, s55, s43
	s_mul_hi_i32 s43, s59, s35
	s_mul_i32 s59, s59, s35
	global_load_dwordx4 v[14:17], v132, s[48:49] nt
	s_add_u32 s48, s54, s59
	s_addc_u32 s49, s55, s43
	s_mul_hi_i32 s43, s60, s35
	s_mul_i32 s60, s60, s35
	global_load_dwordx4 v[26:29], v132, s[48:49] nt
	s_add_u32 s48, s54, s60
	s_addc_u32 s49, s55, s43
	s_mul_hi_i32 s43, s61, s35
	s_mul_i32 s61, s61, s35
	global_load_dwordx4 v[30:33], v132, s[48:49] nt
	s_add_u32 s48, s54, s61
	s_addc_u32 s49, s55, s43
	s_mul_hi_i32 s43, s62, s35
	s_mul_i32 s62, s62, s35
	global_load_dwordx4 v[42:45], v132, s[48:49] nt
	s_add_u32 s48, s54, s62
	s_addc_u32 s49, s55, s43
	s_mul_hi_i32 s43, s63, s35
	s_mul_i32 s63, s63, s35
	global_load_dwordx4 v[22:25], v132, s[48:49] nt
	s_add_u32 s48, s54, s63
	s_addc_u32 s49, s55, s43
	s_mul_hi_i32 s43, s74, s35
	s_mul_i32 s74, s74, s35
	global_load_dwordx4 v[34:37], v132, s[48:49] nt
	s_add_u32 s48, s54, s74
	s_addc_u32 s49, s55, s43
	s_mul_hi_i32 s43, s88, s35
	s_mul_i32 s88, s88, s35
	global_load_dwordx4 v[38:41], v132, s[48:49] nt
	s_add_u32 s48, s54, s88
	s_addc_u32 s49, s55, s43
	s_mul_hi_i32 s43, s89, s35
	s_mul_i32 s89, s89, s35
	global_load_dwordx4 v[50:53], v132, s[48:49] nt
	s_add_u32 s48, s54, s89
	s_waitcnt vmcnt(12)
	v_mul_f32_e32 v66, 0x42800000, v66
	v_mul_f32_e32 v70, 0x42800000, v70
	s_addc_u32 s49, s55, s43
	s_mul_hi_i32 s43, s90, s35
	s_mul_i32 s90, s90, s35
	v_cvt_pk_fp8_f32 v134, v66, v70
	v_mul_f32_e32 v66, 0x42800000, v78
	v_mul_f32_e32 v70, 0x42800000, v86
	global_load_dwordx4 v[46:49], v132, s[48:49] nt
	s_add_u32 s48, s54, s90
	v_cvt_pk_fp8_f32 v135, v66, v70
	v_mul_f32_e32 v66, 0x42800000, v90
	v_mul_f32_e32 v70, 0x42800000, v98
	s_addc_u32 s49, s55, s43
	s_mul_hi_i32 s43, s91, s35
	s_mul_i32 s91, s91, s35
	v_cvt_pk_fp8_f32 v136, v66, v70
	v_mul_f32_e32 v66, 0x42800000, v110
	v_mul_f32_e32 v70, 0x42800000, v118
	global_load_dwordx4 v[54:57], v132, s[48:49] nt
	s_add_u32 s48, s54, s91
	v_mul_f32_e32 v74, 0x42800000, v74
	v_mul_f32_e32 v82, 0x42800000, v82
	v_cvt_pk_fp8_f32 v137, v66, v70
	s_addc_u32 s49, s55, s43
	s_mul_hi_i32 s43, s92, s35
	s_mul_i32 s92, s92, s35
	v_cvt_pk_fp8_f32 v134, v74, v82 op_sel:[0,0,1]
	v_mul_f32_e32 v74, 0x42800000, v94
	v_mul_f32_e32 v78, 0x42800000, v102
	global_load_dwordx4 v[58:61], v132, s[48:49] nt
	s_add_u32 s48, s54, s92
	v_cvt_pk_fp8_f32 v135, v74, v78 op_sel:[0,0,1]
	v_mul_f32_e32 v74, 0x42800000, v106
	v_mul_f32_e32 v78, 0x42800000, v114
	s_addc_u32 s49, s55, s43
	v_cvt_pk_fp8_f32 v136, v74, v78 op_sel:[0,0,1]
	v_mul_f32_e32 v74, 0x42800000, v122
	v_mul_f32_e32 v78, 0x42800000, v126
	global_load_dwordx4 v[62:65], v132, s[48:49] nt
	v_cvt_pk_fp8_f32 v137, v74, v78 op_sel:[0,0,1]
	s_add_i32 s35, s45, 0
	v_mov_b32_e32 v66, s35
	s_movk_i32 s35, 0x240
	v_mad_u32_u24 v66, v133, s35, v66
	s_waitcnt lgkmcnt(0)
	s_barrier
; #define LAS __attribute__((address_space(3)))
; #define GAS __attribute__((address_space(1)))
; __device__ __forceinline__ unsigned pk4_fp8(float a, float b, float c, float d) { int p = 0; p = __builtin_amdgcn_cvt_pk_fp8_f32(a, b, p, false); p = __builtin_amdgcn_cvt_pk_fp8_f32(c, d, p, true); return (unsigned)p; }
; #define WG_BAR() do { LDS_WAIT(); __builtin_amdgcn_s_barrier(); asm volatile("" ::: "memory"); } while (0)
; __device__ __forceinline__ void tr_pack(LAS unsigned char* buf, int wave, int lane, const f32x4 (&v)[16]) {
; #pragma unroll
;     for (int j = 0; j < 4; ++j) { u32x4 o;
; #pragma unroll
;         for (int w = 0; w < 4; ++w) o[w] = pk4_fp8(64.f * v[4 * w][j], 64.f * v[4 * w + 1][j], 64.f * v[4 * w + 2][j], 64.f * v[4 * w + 3][j]);
;         *(LAS u32x4*)(buf + (4 * lane + j) * TRP + 16 * wave) = o; }
; }
; __device__ __forceinline__ void tr_flush(const TrBlk& t, const LAS unsigned char* buf, int wave, int lane) {
; #pragma unroll
;     for (int tt = 0; tt < 4; ++tt) { const int nl = 32 * wave + 8 * tt + (lane >> 3), n = 256 * t.nb + nl;
;         const u32x4 o = *(const LAS u32x4*)(buf + nl * TRP + 16 * (lane & 7));
;         const int drow = t.gu ? ((n >> 7) * 256 + (n & 127) + 128 * t.which) : n;
;         __builtin_nontemporal_store(o, (u32x4 GAS*)(t.dst + (size_t)drow * t.K + 16 * (lane & 7))); }
; template <int NBK> __device__ __forceinline__ void tr_blocks(Ctx& C, int L, int b0) {
;     ...
;     WG_BAR(); tr_flush(t0, buf0, C.wave, C.lane);
;     if (NBK > 1) { tr_pack(buf1, C.wave, C.lane, r1); WG_BAR(); tr_flush(t1, buf1, C.wave, C.lane); }
;     if (NBK > 2) { tr_pack(buf0, C.wave, C.lane, r2); WG_BAR(); tr_flush(t2, buf0, C.wave, C.lane); }
	ds_write_b128 v66, v[134:137]
	v_mul_f32_e32 v67, 0x42800000, v67
	v_mul_f32_e32 v70, 0x42800000, v71
	v_mov_b32_e32 v134, 0
	v_cvt_pk_fp8_f32 v134, v67, v70
	v_mul_f32_e32 v67, 0x42800000, v79
	v_mul_f32_e32 v70, 0x42800000, v87
	v_mov_b32_e32 v135, 0
	v_cvt_pk_fp8_f32 v135, v67, v70
	v_mul_f32_e32 v67, 0x42800000, v91
	v_mul_f32_e32 v70, 0x42800000, v99
	v_mov_b32_e32 v136, 0
	v_cvt_pk_fp8_f32 v136, v67, v70
	v_mul_f32_e32 v67, 0x42800000, v111
	v_mul_f32_e32 v70, 0x42800000, v119
	v_mov_b32_e32 v137, 0
	v_mul_f32_e32 v71, 0x42800000, v75
	v_mul_f32_e32 v74, 0x42800000, v83
	v_cvt_pk_fp8_f32 v137, v67, v70
	v_cvt_pk_fp8_f32 v134, v71, v74 op_sel:[0,0,1]
	v_mul_f32_e32 v71, 0x42800000, v95
	v_mul_f32_e32 v74, 0x42800000, v103
	v_cvt_pk_fp8_f32 v135, v71, v74 op_sel:[0,0,1]
	v_mul_f32_e32 v71, 0x42800000, v107
	v_mul_f32_e32 v74, 0x42800000, v115
	v_cvt_pk_fp8_f32 v136, v71, v74 op_sel:[0,0,1]
	v_mul_f32_e32 v71, 0x42800000, v123
	v_mul_f32_e32 v74, 0x42800000, v127
	v_cvt_pk_fp8_f32 v137, v71, v74 op_sel:[0,0,1]
	v_mul_f32_e32 v67, 0x42800000, v68
	v_mul_f32_e32 v68, 0x42800000, v72
	v_mul_f32_e32 v70, 0x42800000, v76
	ds_write_b128 v66, v[134:137] offset:144
	v_mov_b32_e32 v134, 0
	v_cvt_pk_fp8_f32 v134, v67, v68
	v_mul_f32_e32 v67, 0x42800000, v80
	v_mul_f32_e32 v68, 0x42800000, v88
	v_mov_b32_e32 v135, 0
	v_cvt_pk_fp8_f32 v135, v67, v68
	v_mul_f32_e32 v67, 0x42800000, v92
	v_mul_f32_e32 v68, 0x42800000, v100
	v_mov_b32_e32 v136, 0
	v_cvt_pk_fp8_f32 v136, v67, v68
	v_mul_f32_e32 v67, 0x42800000, v112
	v_mul_f32_e32 v68, 0x42800000, v120
	v_mov_b32_e32 v137, 0
	v_mul_f32_e32 v71, 0x42800000, v84
	v_cvt_pk_fp8_f32 v137, v67, v68
	v_mul_f32_e32 v67, 0x42800000, v69
	v_mul_f32_e32 v69, 0x42800000, v73
	v_mov_b32_e32 v68, 0
	v_cvt_pk_fp8_f32 v134, v70, v71 op_sel:[0,0,1]
	v_mul_f32_e32 v70, 0x42800000, v96
	v_mul_f32_e32 v71, 0x42800000, v104
	v_cvt_pk_fp8_f32 v68, v67, v69
	v_cvt_pk_fp8_f32 v135, v70, v71 op_sel:[0,0,1]
	v_mul_f32_e32 v70, 0x42800000, v108
	v_mul_f32_e32 v71, 0x42800000, v116
	v_cvt_pk_fp8_f32 v136, v70, v71 op_sel:[0,0,1]
	v_mul_f32_e32 v70, 0x42800000, v124
	v_mul_f32_e32 v71, 0x42800000, v128
	v_cvt_pk_fp8_f32 v137, v70, v71 op_sel:[0,0,1]
	v_mul_f32_e32 v70, 0x42800000, v77
	v_mul_f32_e32 v71, 0x42800000, v85
	v_cvt_pk_fp8_f32 v68, v70, v71 op_sel:[0,0,1]
	v_mul_f32_e32 v67, 0x42800000, v81
	v_mul_f32_e32 v70, 0x42800000, v89
	v_mov_b32_e32 v69, 0
	v_cvt_pk_fp8_f32 v69, v67, v70
	v_mul_f32_e32 v71, 0x42800000, v97
	v_mul_f32_e32 v72, 0x42800000, v105
	v_mul_f32_e32 v67, 0x42800000, v93
	v_cvt_pk_fp8_f32 v69, v71, v72 op_sel:[0,0,1]
	v_mul_f32_e32 v71, 0x42800000, v101
	v_mov_b32_e32 v70, 0
	v_cvt_pk_fp8_f32 v70, v67, v71
	v_mul_f32_e32 v72, 0x42800000, v109
	v_mul_f32_e32 v73, 0x42800000, v117
	v_mul_f32_e32 v67, 0x42800000, v113
	v_cvt_pk_fp8_f32 v70, v72, v73 op_sel:[0,0,1]
	v_mul_f32_e32 v72, 0x42800000, v121
	v_mov_b32_e32 v71, 0
	v_cvt_pk_fp8_f32 v71, v67, v72
	v_mul_f32_e32 v73, 0x42800000, v125
	v_mul_f32_e32 v74, 0x42800000, v129
	s_lshl_b32 s24, s24, 5
	v_cvt_pk_fp8_f32 v71, v73, v74 op_sel:[0,0,1]
	v_bfe_u32 v67, v131, 3, 3
	v_or_b32_e32 v76, s24, v67
	s_movk_i32 s35, 0x90
	ds_write_b128 v66, v[134:137] offset:288
	ds_write_b128 v66, v[68:71] offset:432
	v_and_b32_e32 v162, 0x70, v132
	v_add_u32_e32 v72, s44, v76
	v_mul_lo_u32 v68, v76, s35
	s_waitcnt lgkmcnt(0)
	s_barrier
	v_add3_u32 v77, 0, v162, v68
	v_lshlrev_b32_e32 v73, 1, v72
	v_bitop3_b32 v67, s24, v211, v67 bitop3:0xc8
	s_lshl_b32 s24, s34, 7
	ds_read_b128 v[68:71], v77
	v_and_b32_e32 v73, 0xffffff00, v73
	v_or_b32_e32 v74, s24, v67
	v_add_u32_e32 v73, v74, v73
	v_cndmask_b32_e64 v74, v72, v73, s[8:9]
	v_mov_b64_e32 v[72:73], s[46:47]
	v_mad_i64_i32 v[74:75], s[34:35], s11, v74, v[72:73]
	v_lshl_add_u64 v[74:75], v[74:75], 0, v[162:163]
	v_or_b32_e32 v78, 8, v76
	s_waitcnt lgkmcnt(0)
	global_store_dwordx4 v[74:75], v[68:71], off nt
	v_add_u32_e32 v74, s44, v78
	v_lshlrev_b32_e32 v75, 1, v74
	v_bitop3_b32 v79, v76, s83, 8 bitop3:0xc8
	ds_read_b128 v[68:71], v77 offset:1152
	v_and_b32_e32 v75, 0xffffff00, v75
	v_or_b32_e32 v80, s24, v79
	v_add_u32_e32 v75, v80, v75
	v_cndmask_b32_e64 v74, v74, v75, s[8:9]
	v_mad_i64_i32 v[74:75], s[34:35], s11, v74, v[72:73]
	v_lshl_add_u64 v[74:75], v[74:75], 0, v[162:163]
	v_or_b32_e32 v80, 16, v76
	s_waitcnt lgkmcnt(0)
	global_store_dwordx4 v[74:75], v[68:71], off nt
	v_add_u32_e32 v74, s44, v80
	v_lshlrev_b32_e32 v75, 1, v74
	v_bitop3_b32 v81, v76, s84, 16 bitop3:0xc8
	ds_read_b128 v[68:71], v77 offset:2304
	v_and_b32_e32 v75, 0xffffff00, v75
	v_or_b32_e32 v82, s24, v81
	v_add_u32_e32 v75, v82, v75
	v_cndmask_b32_e64 v74, v74, v75, s[8:9]
	v_mad_i64_i32 v[74:75], s[34:35], s11, v74, v[72:73]
	v_lshl_add_u64 v[74:75], v[74:75], 0, v[162:163]
	s_waitcnt lgkmcnt(0)
	global_store_dwordx4 v[74:75], v[68:71], off nt
	v_or_b32_e32 v74, 24, v76
	v_add_u32_e32 v75, s44, v74
	s_movk_i32 s34, 0x7f
	v_lshlrev_b32_e32 v82, 1, v75
	v_bitop3_b32 v83, v76, s34, 24 bitop3:0xc8
	ds_read_b128 v[68:71], v77 offset:3456
	v_and_b32_e32 v82, 0xffffff00, v82
	v_or_b32_e32 v84, s24, v83
	v_add_u32_e32 v82, v84, v82
	v_cndmask_b32_e64 v75, v75, v82, s[8:9]
	v_mad_i64_i32 v[72:73], s[8:9], s11, v75, v[72:73]
	v_lshl_add_u64 v[72:73], v[72:73], 0, v[162:163]
	s_waitcnt lgkmcnt(0)
	global_store_dwordx4 v[72:73], v[68:71], off nt
	s_waitcnt vmcnt(8)
	v_mul_f32_e32 v2, 0x42800000, v2
	v_mul_f32_e32 v6, 0x42800000, v6
	v_mov_b32_e32 v68, v163
	v_cvt_pk_fp8_f32 v68, v2, v6
	v_mul_f32_e32 v2, 0x42800000, v14
	v_mul_f32_e32 v6, 0x42800000, v26
	v_mov_b32_e32 v69, v163
	v_cvt_pk_fp8_f32 v69, v2, v6
	v_mul_f32_e32 v2, 0x42800000, v22
	v_mul_f32_e32 v6, 0x42800000, v34
	v_mov_b32_e32 v70, v163
	v_cvt_pk_fp8_f32 v70, v2, v6
	s_waitcnt vmcnt(7)
; #define LAS __attribute__((address_space(3)))
; #define GAS __attribute__((address_space(1)))
; __device__ __forceinline__ unsigned pk4_fp8(float a, float b, float c, float d) { int p = 0; p = __builtin_amdgcn_cvt_pk_fp8_f32(a, b, p, false); p = __builtin_amdgcn_cvt_pk_fp8_f32(c, d, p, true); return (unsigned)p; }
; __device__ __forceinline__ void tr_pack(LAS unsigned char* buf, int wave, int lane, const f32x4 (&v)[16]) {
; #pragma unroll
;     for (int j = 0; j < 4; ++j) { u32x4 o;
; #pragma unroll
;         for (int w = 0; w < 4; ++w) o[w] = pk4_fp8(64.f * v[4 * w][j], 64.f * v[4 * w + 1][j], 64.f * v[4 * w + 2][j], 64.f * v[4 * w + 3][j]);
;         *(LAS u32x4*)(buf + (4 * lane + j) * TRP + 16 * wave) = o; }
; }
; __device__ __forceinline__ void tr_flush(const TrBlk& t, const LAS unsigned char* buf, int wave, int lane) {
; #pragma unroll
;     for (int tt = 0; tt < 4; ++tt) { const int nl = 32 * wave + 8 * tt + (lane >> 3), n = 256 * t.nb + nl;
;         const u32x4 o = *(const LAS u32x4*)(buf + nl * TRP + 16 * (lane & 7));
;         const int drow = t.gu ? ((n >> 7) * 256 + (n & 127) + 128 * t.which) : n;
;         __builtin_nontemporal_store(o, (u32x4 GAS*)(t.dst + (size_t)drow * t.K + 16 * (lane & 7))); }
	v_mul_f32_e32 v2, 0x42800000, v46
	s_waitcnt vmcnt(6)
	v_mul_f32_e32 v6, 0x42800000, v54
	v_mov_b32_e32 v71, v163
	v_mul_f32_e32 v10, 0x42800000, v10
	v_mul_f32_e32 v18, 0x42800000, v18
	v_cvt_pk_fp8_f32 v71, v2, v6
	v_cvt_pk_fp8_f32 v68, v10, v18 op_sel:[0,0,1]
	v_mul_f32_e32 v10, 0x42800000, v30
	v_mul_f32_e32 v14, 0x42800000, v42
	v_cvt_pk_fp8_f32 v69, v10, v14 op_sel:[0,0,1]
	v_mul_f32_e32 v10, 0x42800000, v38
	v_mul_f32_e32 v14, 0x42800000, v50
	v_cvt_pk_fp8_f32 v70, v10, v14 op_sel:[0,0,1]
	s_waitcnt vmcnt(5)
	v_mul_f32_e32 v10, 0x42800000, v58
	s_waitcnt vmcnt(4)
	v_mul_f32_e32 v14, 0x42800000, v62
	v_cvt_pk_fp8_f32 v71, v10, v14 op_sel:[0,0,1]
	v_mul_f32_e32 v2, 0x42800000, v3
	v_mul_f32_e32 v3, 0x42800000, v7
	v_mul_f32_e32 v6, 0x42800000, v11
	ds_write_b128 v66, v[68:71] offset:36864
	v_mov_b32_e32 v68, v163
	v_cvt_pk_fp8_f32 v68, v2, v3
	v_mul_f32_e32 v2, 0x42800000, v15
	v_mul_f32_e32 v3, 0x42800000, v27
	v_mov_b32_e32 v69, v163
	v_cvt_pk_fp8_f32 v69, v2, v3
	v_mul_f32_e32 v2, 0x42800000, v23
	v_mul_f32_e32 v3, 0x42800000, v35
	v_mov_b32_e32 v70, v163
	v_cvt_pk_fp8_f32 v70, v2, v3
	v_mul_f32_e32 v2, 0x42800000, v47
	v_mul_f32_e32 v3, 0x42800000, v55
	v_mov_b32_e32 v71, v163
	v_mul_f32_e32 v7, 0x42800000, v19
	v_cvt_pk_fp8_f32 v71, v2, v3
	v_cvt_pk_fp8_f32 v68, v6, v7 op_sel:[0,0,1]
	v_mul_f32_e32 v6, 0x42800000, v31
	v_mul_f32_e32 v7, 0x42800000, v43
	v_cvt_pk_fp8_f32 v69, v6, v7 op_sel:[0,0,1]
	v_mul_f32_e32 v6, 0x42800000, v39
	v_mul_f32_e32 v7, 0x42800000, v51
	v_cvt_pk_fp8_f32 v70, v6, v7 op_sel:[0,0,1]
	v_mul_f32_e32 v6, 0x42800000, v59
	v_mul_f32_e32 v7, 0x42800000, v63
	v_cvt_pk_fp8_f32 v71, v6, v7 op_sel:[0,0,1]
	v_mul_f32_e32 v2, 0x42800000, v4
	v_mul_f32_e32 v3, 0x42800000, v8
	v_mul_f32_e32 v4, 0x42800000, v12
	ds_write_b128 v66, v[68:71] offset:37008
	v_mov_b32_e32 v68, v163
	v_cvt_pk_fp8_f32 v68, v2, v3
	v_mul_f32_e32 v2, 0x42800000, v16
	v_mul_f32_e32 v3, 0x42800000, v28
	v_mov_b32_e32 v69, v163
	v_cvt_pk_fp8_f32 v69, v2, v3
	v_mul_f32_e32 v2, 0x42800000, v24
	v_mul_f32_e32 v3, 0x42800000, v36
	v_mov_b32_e32 v70, v163
	v_cvt_pk_fp8_f32 v70, v2, v3
	v_mul_f32_e32 v2, 0x42800000, v48
	v_mul_f32_e32 v3, 0x42800000, v56
	v_mov_b32_e32 v71, v163
	v_mul_f32_e32 v6, 0x42800000, v20
	v_cvt_pk_fp8_f32 v71, v2, v3
	v_cvt_pk_fp8_f32 v68, v4, v6 op_sel:[0,0,1]
	v_mul_f32_e32 v4, 0x42800000, v32
	v_mul_f32_e32 v6, 0x42800000, v44
	v_cvt_pk_fp8_f32 v69, v4, v6 op_sel:[0,0,1]
	v_mul_f32_e32 v4, 0x42800000, v40
	v_mul_f32_e32 v6, 0x42800000, v52
	v_cvt_pk_fp8_f32 v70, v4, v6 op_sel:[0,0,1]
	v_mul_f32_e32 v4, 0x42800000, v60
	v_mul_f32_e32 v6, 0x42800000, v64
	v_cvt_pk_fp8_f32 v71, v4, v6 op_sel:[0,0,1]
	v_mul_f32_e32 v3, 0x42800000, v5
	v_mul_f32_e32 v4, 0x42800000, v9
	v_mov_b32_e32 v2, v163
	v_cvt_pk_fp8_f32 v2, v3, v4
	v_mul_f32_e32 v5, 0x42800000, v13
	v_mul_f32_e32 v6, 0x42800000, v21
	v_mul_f32_e32 v4, 0x42800000, v17
	v_cvt_pk_fp8_f32 v2, v5, v6 op_sel:[0,0,1]
	v_mul_f32_e32 v5, 0x42800000, v29
	v_mov_b32_e32 v3, v163
	v_cvt_pk_fp8_f32 v3, v4, v5
	v_mul_f32_e32 v6, 0x42800000, v33
	v_mul_f32_e32 v7, 0x42800000, v45
	v_mul_f32_e32 v5, 0x42800000, v25
	v_cvt_pk_fp8_f32 v3, v6, v7 op_sel:[0,0,1]
	v_mul_f32_e32 v6, 0x42800000, v37
	v_mov_b32_e32 v4, v163
	v_cvt_pk_fp8_f32 v4, v5, v6
	v_mul_f32_e32 v7, 0x42800000, v41
	v_mul_f32_e32 v8, 0x42800000, v53
	v_mul_f32_e32 v6, 0x42800000, v49
	v_cvt_pk_fp8_f32 v4, v7, v8 op_sel:[0,0,1]
	v_mul_f32_e32 v7, 0x42800000, v57
	v_mov_b32_e32 v5, v163
	v_cvt_pk_fp8_f32 v5, v6, v7
	v_mul_f32_e32 v8, 0x42800000, v61
	v_mul_f32_e32 v9, 0x42800000, v65
	ds_write_b128 v66, v[68:71] offset:37152
	v_cvt_pk_fp8_f32 v5, v8, v9 op_sel:[0,0,1]
	v_add_u32_e32 v6, s10, v76
	v_lshlrev_b32_e32 v7, 1, v6
	s_lshl_b32 s11, s18, 7
	ds_write_b128 v66, v[2:5] offset:37296
	s_waitcnt lgkmcnt(0)
	s_barrier
	ds_read_b128 v[2:5], v77 offset:36864
	v_and_b32_e32 v7, 0xffffff00, v7
	v_or_b32_e32 v8, s11, v67
	v_add_u32_e32 v7, v8, v7
	v_cndmask_b32_e64 v8, v6, v7, s[6:7]
	v_mov_b64_e32 v[6:7], s[12:13]
	v_mad_i64_i32 v[8:9], s[8:9], s19, v8, v[6:7]
	v_lshl_add_u64 v[8:9], v[8:9], 0, v[162:163]
	s_waitcnt lgkmcnt(0)
	global_store_dwordx4 v[8:9], v[2:5], off nt
	v_add_u32_e32 v8, s10, v78
	v_lshlrev_b32_e32 v9, 1, v8
	ds_read_b128 v[2:5], v77 offset:38016
	v_and_b32_e32 v9, 0xffffff00, v9
	v_or_b32_e32 v10, s11, v79
	v_add_u32_e32 v9, v10, v9
	v_cndmask_b32_e64 v8, v8, v9, s[6:7]
	v_mad_i64_i32 v[8:9], s[8:9], s19, v8, v[6:7]
	v_lshl_add_u64 v[8:9], v[8:9], 0, v[162:163]
	s_waitcnt lgkmcnt(0)
	global_store_dwordx4 v[8:9], v[2:5], off nt
	v_add_u32_e32 v8, s10, v80
	v_lshlrev_b32_e32 v9, 1, v8
	ds_read_b128 v[2:5], v77 offset:39168
	v_and_b32_e32 v9, 0xffffff00, v9
	v_or_b32_e32 v10, s11, v81
	v_add_u32_e32 v9, v10, v9
	v_cndmask_b32_e64 v8, v8, v9, s[6:7]
	v_mad_i64_i32 v[8:9], s[8:9], s19, v8, v[6:7]
	v_lshl_add_u64 v[8:9], v[8:9], 0, v[162:163]
	s_waitcnt lgkmcnt(0)
	global_store_dwordx4 v[8:9], v[2:5], off nt
	v_add_u32_e32 v8, s10, v74
	v_lshlrev_b32_e32 v9, 1, v8
	ds_read_b128 v[2:5], v77 offset:40320
	v_and_b32_e32 v9, 0xffffff00, v9
	v_or_b32_e32 v10, s11, v83
	v_add_u32_e32 v9, v10, v9
	v_cndmask_b32_e64 v8, v8, v9, s[6:7]
	v_mad_i64_i32 v[6:7], s[6:7], s19, v8, v[6:7]
	v_lshl_add_u64 v[6:7], v[6:7], 0, v[162:163]
	s_waitcnt lgkmcnt(0)
	global_store_dwordx4 v[6:7], v[2:5], off nt
	s_barrier
	s_and_saveexec_b64 s[6:7], s[4:5]
	s_cbranch_execz .LBB0_873
	s_waitcnt vmcnt(8)
	v_add_u32_e32 v2, s64, v243
	v_cmp_eq_u32_e32 vcc, -1, v130
	s_nop 1
	v_cndmask_b32_e32 v130, v130, v2, vcc
	v_mov_b32_e32 v2, s85
	ds_write_b32 v2, v130
	s_branch .LBB0_873

; #define GAS __attribute__((address_space(1)))
; __device__ __forceinline__ void tr_load(const TrBlk& t, int wave, int lane, f32x4 (&v)[16]) {
; #pragma unroll
;     for (int i = 0; i < 16; ++i) v[i] = __builtin_nontemporal_load((const f32x4 GAS*)((const char GAS*)t.src + (size_t)(16 * wave + i) * t.N * 4 + 16u * lane));
; template <int NBK> __device__ __forceinline__ void tr_blocks(Ctx& C, int L, int b0) {
;     ...
;     const TrBlk t0 = tr_decode(C, L, b0), t1 = tr_decode(C, L, b0 + (NBK > 1 ? 1 : 0)), t2 = tr_decode(C, L, b0 + (NBK > 2 ? 2 : 0)), t3 = tr_decode(C, L, b0 + (NBK > 3 ? 3 : 0));
;     tr_load(t0, C.wave, C.lane, r0); if (NBK > 1) tr_load(t1, C.wave, C.lane, r1); if (NBK > 2) tr_load(t2, C.wave, C.lane, r2);
.LBB0_2152:
	s_ashr_i32 s24, s87, 6
	s_add_u32 s10, s10, s56
	s_addc_u32 s11, s11, s57
	s_and_b64 s[56:57], s[6:7], exec
	s_cselect_b32 s19, s80, 0x1b200000
	s_and_b64 s[52:53], s[52:53], exec
	s_cselect_b32 s19, 0x2200000, s19
	s_and_b64 s[52:53], s[54:55], exec
	s_cselect_b32 s19, 0x400000, s19
	s_add_u32 s56, s48, s19
	s_addc_u32 s57, s49, 0
	s_cmp_eq_u32 s18, 2
	s_cselect_b64 s[52:53], -1, 0
	s_and_b64 s[52:53], s[12:13], s[52:53]
	s_and_b64 s[52:53], s[52:53], exec
	s_cselect_b32 s19, s79, 0x800
	s_add_i32 s97, s97, 32
	s_and_b64 s[52:53], s[12:13], exec
	s_cselect_b32 s52, s97, 1
	s_mul_i32 s58, s19, s52
	s_mul_hi_i32 s59, s19, s52
	s_and_b64 s[52:53], s[6:7], exec
	s_cselect_b32 s60, 0x600, s76
	s_and_b64 s[52:53], s[54:55], exec
	s_cselect_b32 s52, 0xf00, s60
	s_mul_i32 s53, s59, s52
	s_mul_hi_u32 s54, s58, s52
	s_add_i32 s54, s54, s53
	s_mul_i32 s52, s58, s52
	s_add_u32 s52, s56, s52
	s_mul_i32 s96, s96, 48
	s_addc_u32 s53, s57, s54
	s_sub_i32 s54, s95, s96
	s_and_b64 s[12:13], s[12:13], exec
	s_cselect_b32 s54, s54, s94
	s_abs_i32 s55, s93
	v_cvt_f32_u32_e32 v2, s55
	s_sub_i32 s56, 0, s55
	s_abs_i32 s13, s54
	s_xor_b32 s12, s54, s93
	v_rcp_iflag_f32_e32 v2, v2
	s_ashr_i32 s12, s12, 31
	s_load_dwordx2 s[10:11], s[10:11], 0x0
	s_mul_i32 s59, s59, s35
	v_mul_f32_e32 v2, 0x4f7ffffe, v2
	v_cvt_u32_f32_e32 v2, v2
	s_mul_i32 s91, s91, 48
	v_and_b32_e32 v133, 63, v131
	v_lshlrev_b32_e32 v132, 4, v133
	v_readfirstlane_b32 s57, v2
	s_mul_i32 s56, s56, s57
	s_mul_hi_u32 s56, s57, s56
	s_add_i32 s57, s57, s56
	s_mul_hi_u32 s56, s13, s57
	s_mul_i32 s57, s56, s55
	s_sub_i32 s13, s13, s57
	s_add_i32 s57, s56, 1
	s_sub_i32 s60, s13, s55
	s_cmp_ge_u32 s13, s55
	s_cselect_b32 s56, s57, s56
	s_cselect_b32 s13, s60, s13
	s_add_i32 s57, s56, 1
	s_cmp_ge_u32 s13, s55
	s_cselect_b32 s13, s57, s56
	s_xor_b32 s13, s13, s12
	s_sub_i32 s55, s13, s12
	s_lshl_b32 s56, s55, 7
	s_ashr_i32 s13, s56, 31
	s_add_u32 s12, s52, s56
	s_mul_hi_u32 s52, s58, s35
	s_addc_u32 s13, s53, s13
	s_add_i32 s53, s52, s59
	s_mul_i32 s52, s58, s35
	s_lshl_b64 s[52:53], s[52:53], 2
	s_waitcnt lgkmcnt(0)
	s_add_u32 s52, s10, s52
	s_addc_u32 s53, s11, s53
	s_mul_hi_i32 s11, s56, s35
	s_mul_i32 s10, s56, s35
	s_lshl_b64 s[10:11], s[10:11], 2
	s_add_u32 s56, s52, s10
	s_mul_i32 s55, s55, s93
	s_addc_u32 s57, s53, s11
	s_sub_i32 s10, s54, s55
	s_lshl_b32 s10, s10, 8
	s_ashr_i32 s11, s10, 31
	s_lshl_b64 s[52:53], s[10:11], 2
	s_add_u32 s52, s56, s52
	s_addc_u32 s53, s57, s53
	s_and_b64 s[54:55], s[8:9], exec
	s_cselect_b32 s11, s80, 0x1b200000
	s_and_b64 s[44:45], s[44:45], exec
	s_cselect_b32 s11, 0x2200000, s11
	s_and_b64 s[44:45], s[46:47], exec
	s_cselect_b32 s11, 0x400000, s11
	s_add_u32 s48, s48, s11
	s_addc_u32 s49, s49, 0
	s_cmp_eq_u32 s34, 2
	s_cselect_b64 s[44:45], -1, 0
	s_and_b64 s[44:45], s[42:43], s[44:45]
	s_and_b64 s[44:45], s[44:45], exec
	s_cselect_b32 s11, s79, 0x800
	s_add_i32 s92, s92, 32
	s_and_b64 s[44:45], s[42:43], exec
	s_cselect_b32 s44, s92, 1
	s_mul_i32 s54, s11, s44
	s_mul_hi_i32 s55, s11, s44
	s_and_b64 s[44:45], s[8:9], exec
	s_cselect_b32 s56, 0x600, s76
	s_and_b64 s[44:45], s[46:47], exec
	s_cselect_b32 s44, 0xf00, s56
	s_mul_i32 s45, s55, s44
	s_mul_hi_u32 s46, s54, s44
	s_add_i32 s46, s46, s45
	s_mul_i32 s44, s54, s44
	s_add_u32 s44, s48, s44
	s_addc_u32 s45, s49, s46
	s_sub_i32 s46, s90, s91
	s_and_b64 s[42:43], s[42:43], exec
	s_cselect_b32 s46, s46, s89
	s_abs_i32 s47, s88
	v_cvt_f32_u32_e32 v2, s47
	s_sub_i32 s48, 0, s47
	s_abs_i32 s43, s46
	s_xor_b32 s42, s46, s88
	v_rcp_iflag_f32_e32 v2, v2
	s_ashr_i32 s42, s42, 31
	s_mul_i32 s55, s55, s74
	v_mov_b32_e32 v134, 0
	v_mul_f32_e32 v2, 0x4f7ffffe, v2
	v_cvt_u32_f32_e32 v2, v2
	v_mov_b32_e32 v135, 0
	v_mov_b32_e32 v136, 0
	v_mov_b32_e32 v137, 0
	v_readfirstlane_b32 s49, v2
	s_mul_i32 s48, s48, s49
	s_mul_hi_u32 s48, s49, s48
	s_add_i32 s49, s49, s48
	s_mul_hi_u32 s48, s43, s49
	s_mul_i32 s49, s48, s47
	s_sub_i32 s43, s43, s49
	s_add_i32 s49, s48, 1
	s_sub_i32 s56, s43, s47
	s_cmp_ge_u32 s43, s47
	s_cselect_b32 s48, s49, s48
	s_cselect_b32 s43, s56, s43
	s_add_i32 s49, s48, 1
	s_cmp_ge_u32 s43, s47
	s_cselect_b32 s43, s49, s48
	s_xor_b32 s43, s43, s42
	s_sub_i32 s47, s43, s42
	s_lshl_b32 s48, s47, 7
	s_ashr_i32 s42, s48, 31
	s_add_u32 s44, s44, s48
	s_addc_u32 s45, s45, s42
	s_mul_hi_u32 s42, s54, s74
	s_add_i32 s43, s42, s55
	s_mul_i32 s42, s54, s74
	s_lshl_b64 s[42:43], s[42:43], 2
	s_add_u32 s49, s50, s42
	s_addc_u32 s50, s51, s43
	s_mul_hi_i32 s43, s48, s74
	s_mul_i32 s42, s48, s74
	s_lshl_b64 s[42:43], s[42:43], 2
	s_add_u32 s48, s49, s42
	s_mul_i32 s47, s47, s88
	s_addc_u32 s49, s50, s43
	s_sub_i32 s42, s46, s47
	s_lshl_b32 s42, s42, 8
	s_ashr_i32 s43, s42, 31
	s_lshl_b64 s[46:47], s[42:43], 2
	s_add_u32 s48, s48, s46
	s_addc_u32 s49, s49, s47
	s_and_b32 s50, s87, 0xffffffc0
	s_lshl_b32 s43, s24, 4
	s_mul_i32 s46, s50, s74
	s_mul_hi_i32 s47, s50, s74
	s_add_u32 s46, s48, s46
	s_addc_u32 s47, s49, s47
	s_or_b32 s51, s50, 4
	global_load_dwordx4 v[66:69], v132, s[46:47] nt
	s_mul_i32 s46, s51, s74
	s_mul_hi_i32 s47, s51, s74
	s_add_u32 s46, s48, s46
	s_addc_u32 s47, s49, s47
	s_or_b32 s54, s50, 8
	global_load_dwordx4 v[70:73], v132, s[46:47] nt
	s_mul_i32 s46, s54, s74
	s_mul_hi_i32 s47, s54, s74
	s_add_u32 s46, s48, s46
	s_addc_u32 s47, s49, s47
	s_or_b32 s55, s50, 12
	global_load_dwordx4 v[74:77], v132, s[46:47] nt
	s_mul_i32 s46, s55, s74
	s_mul_hi_i32 s47, s55, s74
	s_add_u32 s46, s48, s46
	s_addc_u32 s47, s49, s47
	s_or_b32 s56, s50, 16
	global_load_dwordx4 v[82:85], v132, s[46:47] nt
	s_mul_i32 s46, s56, s74
	s_mul_hi_i32 s47, s56, s74
	s_add_u32 s46, s48, s46
	s_addc_u32 s47, s49, s47
; #define LAS __attribute__((address_space(3)))
; #define GAS __attribute__((address_space(1)))
; __device__ __forceinline__ unsigned pk4_fp8(float a, float b, float c, float d) { int p = 0; p = __builtin_amdgcn_cvt_pk_fp8_f32(a, b, p, false); p = __builtin_amdgcn_cvt_pk_fp8_f32(c, d, p, true); return (unsigned)p; }
; #define WG_BAR() do { LDS_WAIT(); __builtin_amdgcn_s_barrier(); asm volatile("" ::: "memory"); } while (0)
; __device__ __forceinline__ void tr_load(const TrBlk& t, int wave, int lane, f32x4 (&v)[16]) {
; #pragma unroll
;     for (int i = 0; i < 16; ++i) v[i] = __builtin_nontemporal_load((const f32x4 GAS*)((const char GAS*)t.src + (size_t)(16 * wave + i) * t.N * 4 + 16u * lane));
; }
; __device__ __forceinline__ void tr_pack(LAS unsigned char* buf, int wave, int lane, const f32x4 (&v)[16]) {
; #pragma unroll
;     for (int j = 0; j < 4; ++j) { u32x4 o;
; #pragma unroll
;         for (int w = 0; w < 4; ++w) o[w] = pk4_fp8(64.f * v[4 * w][j], 64.f * v[4 * w + 1][j], 64.f * v[4 * w + 2][j], 64.f * v[4 * w + 3][j]);
;         *(LAS u32x4*)(buf + (4 * lane + j) * TRP + 16 * wave) = o; }
; template <int NBK> __device__ __forceinline__ void tr_blocks(Ctx& C, int L, int b0) {
;     ...
;     tr_load(t0, C.wave, C.lane, r0); if (NBK > 1) tr_load(t1, C.wave, C.lane, r1); if (NBK > 2) tr_load(t2, C.wave, C.lane, r2);
;     WG_BAR();
;     tr_pack(buf0, C.wave, C.lane, r0);
	s_or_b32 s57, s50, 20
	global_load_dwordx4 v[78:81], v132, s[46:47] nt
	s_mul_i32 s46, s57, s74
	s_mul_hi_i32 s47, s57, s74
	s_add_u32 s46, s48, s46
	s_addc_u32 s47, s49, s47
	s_or_b32 s58, s50, 24
	global_load_dwordx4 v[86:89], v132, s[46:47] nt
	s_mul_i32 s46, s58, s74
	s_mul_hi_i32 s47, s58, s74
	s_add_u32 s46, s48, s46
	s_addc_u32 s47, s49, s47
	s_or_b32 s59, s50, 28
	global_load_dwordx4 v[94:97], v132, s[46:47] nt
	s_mul_i32 s46, s59, s74
	s_mul_hi_i32 s47, s59, s74
	s_add_u32 s46, s48, s46
	s_addc_u32 s47, s49, s47
	s_or_b32 s60, s50, 32
	global_load_dwordx4 v[102:105], v132, s[46:47] nt
	s_mul_i32 s46, s60, s74
	s_mul_hi_i32 s47, s60, s74
	s_add_u32 s46, s48, s46
	s_addc_u32 s47, s49, s47
	s_or_b32 s61, s50, 36
	global_load_dwordx4 v[90:93], v132, s[46:47] nt
	s_mul_i32 s46, s61, s74
	s_mul_hi_i32 s47, s61, s74
	s_add_u32 s46, s48, s46
	s_addc_u32 s47, s49, s47
	s_or_b32 s87, s50, 40
	global_load_dwordx4 v[98:101], v132, s[46:47] nt
	s_mul_i32 s46, s87, s74
	s_mul_hi_i32 s47, s87, s74
	s_add_u32 s46, s48, s46
	s_addc_u32 s47, s49, s47
	s_or_b32 s88, s50, 44
	global_load_dwordx4 v[106:109], v132, s[46:47] nt
	s_mul_i32 s46, s88, s74
	s_mul_hi_i32 s47, s88, s74
	s_add_u32 s46, s48, s46
	s_addc_u32 s47, s49, s47
	s_or_b32 s89, s50, 48
	global_load_dwordx4 v[114:117], v132, s[46:47] nt
	s_mul_i32 s46, s89, s74
	s_mul_hi_i32 s47, s89, s74
	s_add_u32 s46, s48, s46
	s_addc_u32 s47, s49, s47
	s_or_b32 s90, s50, 52
	global_load_dwordx4 v[110:113], v132, s[46:47] nt
	s_mul_i32 s46, s90, s74
	s_mul_hi_i32 s47, s90, s74
	s_add_u32 s46, s48, s46
	s_addc_u32 s47, s49, s47
	s_or_b32 s91, s50, 56
	global_load_dwordx4 v[118:121], v132, s[46:47] nt
	s_mul_i32 s46, s91, s74
	s_mul_hi_i32 s47, s91, s74
	s_add_u32 s46, s48, s46
	s_addc_u32 s47, s49, s47
	s_or_b32 s92, s50, 60
	global_load_dwordx4 v[122:125], v132, s[46:47] nt
	s_mul_i32 s46, s92, s74
	s_mul_hi_i32 s47, s92, s74
	s_add_u32 s46, s48, s46
	s_addc_u32 s47, s49, s47
	global_load_dwordx4 v[126:129], v132, s[46:47] nt
	s_mul_hi_i32 s47, s50, s35
	s_mul_i32 s50, s50, s35
	s_add_u32 s46, s52, s50
	s_addc_u32 s47, s53, s47
	global_load_dwordx4 v[2:5], v132, s[46:47] nt
	s_mul_hi_i32 s47, s51, s35
	s_mul_i32 s51, s51, s35
	s_add_u32 s46, s52, s51
	s_addc_u32 s47, s53, s47
	global_load_dwordx4 v[6:9], v132, s[46:47] nt
	s_mul_hi_i32 s47, s54, s35
	s_mul_i32 s54, s54, s35
	s_add_u32 s46, s52, s54
	s_addc_u32 s47, s53, s47
	global_load_dwordx4 v[10:13], v132, s[46:47] nt
	s_mul_hi_i32 s47, s55, s35
	s_mul_i32 s55, s55, s35
	s_add_u32 s46, s52, s55
	s_addc_u32 s47, s53, s47
	global_load_dwordx4 v[18:21], v132, s[46:47] nt
	s_mul_hi_i32 s47, s56, s35
	s_mul_i32 s56, s56, s35
	s_add_u32 s46, s52, s56
	s_addc_u32 s47, s53, s47
	global_load_dwordx4 v[14:17], v132, s[46:47] nt
	s_mul_hi_i32 s47, s57, s35
	s_mul_i32 s57, s57, s35
	s_add_u32 s46, s52, s57
	s_addc_u32 s47, s53, s47
	global_load_dwordx4 v[26:29], v132, s[46:47] nt
	s_mul_hi_i32 s47, s58, s35
	s_mul_i32 s58, s58, s35
	s_add_u32 s46, s52, s58
	s_addc_u32 s47, s53, s47
	global_load_dwordx4 v[30:33], v132, s[46:47] nt
	s_mul_hi_i32 s47, s59, s35
	s_mul_i32 s59, s59, s35
	s_add_u32 s46, s52, s59
	s_addc_u32 s47, s53, s47
	global_load_dwordx4 v[42:45], v132, s[46:47] nt
	s_mul_hi_i32 s47, s60, s35
	s_mul_i32 s60, s60, s35
	s_add_u32 s46, s52, s60
	s_addc_u32 s47, s53, s47
	global_load_dwordx4 v[22:25], v132, s[46:47] nt
	s_mul_hi_i32 s47, s61, s35
	s_mul_i32 s61, s61, s35
	s_add_u32 s46, s52, s61
	s_addc_u32 s47, s53, s47
	global_load_dwordx4 v[34:37], v132, s[46:47] nt
	s_mul_hi_i32 s47, s87, s35
	s_mul_i32 s87, s87, s35
	s_add_u32 s46, s52, s87
	s_addc_u32 s47, s53, s47
	global_load_dwordx4 v[38:41], v132, s[46:47] nt
	s_mul_hi_i32 s47, s88, s35
	s_mul_i32 s88, s88, s35
	s_add_u32 s46, s52, s88
	s_addc_u32 s47, s53, s47
	global_load_dwordx4 v[50:53], v132, s[46:47] nt
	s_mul_hi_i32 s47, s89, s35
	s_mul_i32 s89, s89, s35
	s_add_u32 s46, s52, s89
	s_addc_u32 s47, s53, s47
	global_load_dwordx4 v[46:49], v132, s[46:47] nt
	s_mul_hi_i32 s47, s90, s35
	s_mul_i32 s90, s90, s35
	s_add_u32 s46, s52, s90
	s_waitcnt vmcnt(13)
	v_mul_f32_e32 v66, 0x42800000, v66
	v_mul_f32_e32 v70, 0x42800000, v70
	s_addc_u32 s47, s53, s47
	v_cvt_pk_fp8_f32 v134, v66, v70
	v_mul_f32_e32 v66, 0x42800000, v78
	v_mul_f32_e32 v70, 0x42800000, v86
	global_load_dwordx4 v[54:57], v132, s[46:47] nt
	s_mul_hi_i32 s47, s91, s35
	s_mul_i32 s91, s91, s35
	v_cvt_pk_fp8_f32 v135, v66, v70
	v_mul_f32_e32 v66, 0x42800000, v90
	v_mul_f32_e32 v70, 0x42800000, v98
	s_add_u32 s46, s52, s91
	v_cvt_pk_fp8_f32 v136, v66, v70
	v_mul_f32_e32 v66, 0x42800000, v110
	v_mul_f32_e32 v70, 0x42800000, v118
	s_addc_u32 s47, s53, s47
	v_mul_f32_e32 v74, 0x42800000, v74
	v_mul_f32_e32 v82, 0x42800000, v82
	v_cvt_pk_fp8_f32 v137, v66, v70
	global_load_dwordx4 v[58:61], v132, s[46:47] nt
	s_mul_hi_i32 s47, s92, s35
	s_mul_i32 s92, s92, s35
	v_cvt_pk_fp8_f32 v134, v74, v82 op_sel:[0,0,1]
	v_mul_f32_e32 v74, 0x42800000, v94
	v_mul_f32_e32 v78, 0x42800000, v102
	s_add_u32 s46, s52, s92
	v_cvt_pk_fp8_f32 v135, v74, v78 op_sel:[0,0,1]
	v_mul_f32_e32 v74, 0x42800000, v106
	v_mul_f32_e32 v78, 0x42800000, v114
	s_addc_u32 s47, s53, s47
	v_cvt_pk_fp8_f32 v136, v74, v78 op_sel:[0,0,1]
	v_mul_f32_e32 v74, 0x42800000, v122
	v_mul_f32_e32 v78, 0x42800000, v126
	global_load_dwordx4 v[62:65], v132, s[46:47] nt
	v_cvt_pk_fp8_f32 v137, v74, v78 op_sel:[0,0,1]
	s_add_i32 s35, s43, 0
	v_mov_b32_e32 v66, s35
	s_movk_i32 s35, 0x240
	v_mad_u32_u24 v66, v133, s35, v66
	s_waitcnt lgkmcnt(0)
	s_barrier
; #define LAS __attribute__((address_space(3)))
; #define GAS __attribute__((address_space(1)))
; __device__ __forceinline__ unsigned pk4_fp8(float a, float b, float c, float d) { int p = 0; p = __builtin_amdgcn_cvt_pk_fp8_f32(a, b, p, false); p = __builtin_amdgcn_cvt_pk_fp8_f32(c, d, p, true); return (unsigned)p; }
; #define WG_BAR() do { LDS_WAIT(); __builtin_amdgcn_s_barrier(); asm volatile("" ::: "memory"); } while (0)
; __device__ __forceinline__ void tr_pack(LAS unsigned char* buf, int wave, int lane, const f32x4 (&v)[16]) {
; #pragma unroll
;     for (int j = 0; j < 4; ++j) { u32x4 o;
; #pragma unroll
;         for (int w = 0; w < 4; ++w) o[w] = pk4_fp8(64.f * v[4 * w][j], 64.f * v[4 * w + 1][j], 64.f * v[4 * w + 2][j], 64.f * v[4 * w + 3][j]);
;         *(LAS u32x4*)(buf + (4 * lane + j) * TRP + 16 * wave) = o; }
; }
; __device__ __forceinline__ void tr_flush(const TrBlk& t, const LAS unsigned char* buf, int wave, int lane) {
; #pragma unroll
;     for (int tt = 0; tt < 4; ++tt) { const int nl = 32 * wave + 8 * tt + (lane >> 3), n = 256 * t.nb + nl;
;         const u32x4 o = *(const LAS u32x4*)(buf + nl * TRP + 16 * (lane & 7));
;         const int drow = t.gu ? ((n >> 7) * 256 + (n & 127) + 128 * t.which) : n;
;         __builtin_nontemporal_store(o, (u32x4 GAS*)(t.dst + (size_t)drow * t.K + 16 * (lane & 7))); }
; template <int NBK> __device__ __forceinline__ void tr_blocks(Ctx& C, int L, int b0) {
;     ...
;     WG_BAR(); tr_flush(t0, buf0, C.wave, C.lane);
;     if (NBK > 1) { tr_pack(buf1, C.wave, C.lane, r1); WG_BAR(); tr_flush(t1, buf1, C.wave, C.lane); }
;     if (NBK > 2) { tr_pack(buf0, C.wave, C.lane, r2); WG_BAR(); tr_flush(t2, buf0, C.wave, C.lane); }
	ds_write_b128 v66, v[134:137]
	v_mul_f32_e32 v67, 0x42800000, v67
	v_mul_f32_e32 v70, 0x42800000, v71
	v_mov_b32_e32 v134, 0
	v_cvt_pk_fp8_f32 v134, v67, v70
	v_mul_f32_e32 v67, 0x42800000, v79
	v_mul_f32_e32 v70, 0x42800000, v87
	v_mov_b32_e32 v135, 0
	v_cvt_pk_fp8_f32 v135, v67, v70
	v_mul_f32_e32 v67, 0x42800000, v91
	v_mul_f32_e32 v70, 0x42800000, v99
	v_mov_b32_e32 v136, 0
	v_cvt_pk_fp8_f32 v136, v67, v70
	v_mul_f32_e32 v67, 0x42800000, v111
	v_mul_f32_e32 v70, 0x42800000, v119
	v_mov_b32_e32 v137, 0
	v_mul_f32_e32 v71, 0x42800000, v75
	v_mul_f32_e32 v74, 0x42800000, v83
	v_cvt_pk_fp8_f32 v137, v67, v70
	v_cvt_pk_fp8_f32 v134, v71, v74 op_sel:[0,0,1]
	v_mul_f32_e32 v71, 0x42800000, v95
	v_mul_f32_e32 v74, 0x42800000, v103
	v_cvt_pk_fp8_f32 v135, v71, v74 op_sel:[0,0,1]
	v_mul_f32_e32 v71, 0x42800000, v107
	v_mul_f32_e32 v74, 0x42800000, v115
	v_cvt_pk_fp8_f32 v136, v71, v74 op_sel:[0,0,1]
	v_mul_f32_e32 v71, 0x42800000, v123
	v_mul_f32_e32 v74, 0x42800000, v127
	v_cvt_pk_fp8_f32 v137, v71, v74 op_sel:[0,0,1]
	v_mul_f32_e32 v67, 0x42800000, v68
	v_mul_f32_e32 v68, 0x42800000, v72
	v_mul_f32_e32 v70, 0x42800000, v76
	ds_write_b128 v66, v[134:137] offset:144
	v_mov_b32_e32 v134, 0
	v_cvt_pk_fp8_f32 v134, v67, v68
	v_mul_f32_e32 v67, 0x42800000, v80
	v_mul_f32_e32 v68, 0x42800000, v88
	v_mov_b32_e32 v135, 0
	v_cvt_pk_fp8_f32 v135, v67, v68
	v_mul_f32_e32 v67, 0x42800000, v92
	v_mul_f32_e32 v68, 0x42800000, v100
	v_mov_b32_e32 v136, 0
	v_cvt_pk_fp8_f32 v136, v67, v68
	v_mul_f32_e32 v67, 0x42800000, v112
	v_mul_f32_e32 v68, 0x42800000, v120
	v_mov_b32_e32 v137, 0
	v_mul_f32_e32 v71, 0x42800000, v84
	v_cvt_pk_fp8_f32 v137, v67, v68
	v_mul_f32_e32 v67, 0x42800000, v69
	v_mul_f32_e32 v69, 0x42800000, v73
	v_mov_b32_e32 v68, 0
	v_cvt_pk_fp8_f32 v134, v70, v71 op_sel:[0,0,1]
	v_mul_f32_e32 v70, 0x42800000, v96
	v_mul_f32_e32 v71, 0x42800000, v104
	v_cvt_pk_fp8_f32 v68, v67, v69
	v_cvt_pk_fp8_f32 v135, v70, v71 op_sel:[0,0,1]
	v_mul_f32_e32 v70, 0x42800000, v108
	v_mul_f32_e32 v71, 0x42800000, v116
	v_cvt_pk_fp8_f32 v136, v70, v71 op_sel:[0,0,1]
	v_mul_f32_e32 v70, 0x42800000, v124
	v_mul_f32_e32 v71, 0x42800000, v128
	v_cvt_pk_fp8_f32 v137, v70, v71 op_sel:[0,0,1]
	v_mul_f32_e32 v70, 0x42800000, v77
	v_mul_f32_e32 v71, 0x42800000, v85
	v_cvt_pk_fp8_f32 v68, v70, v71 op_sel:[0,0,1]
	v_mul_f32_e32 v67, 0x42800000, v81
	v_mul_f32_e32 v70, 0x42800000, v89
	v_mov_b32_e32 v69, 0
	v_cvt_pk_fp8_f32 v69, v67, v70
	v_mul_f32_e32 v71, 0x42800000, v97
	v_mul_f32_e32 v72, 0x42800000, v105
	v_mul_f32_e32 v67, 0x42800000, v93
	v_cvt_pk_fp8_f32 v69, v71, v72 op_sel:[0,0,1]
	v_mul_f32_e32 v71, 0x42800000, v101
	v_mov_b32_e32 v70, 0
	v_cvt_pk_fp8_f32 v70, v67, v71
	v_mul_f32_e32 v72, 0x42800000, v109
	v_mul_f32_e32 v73, 0x42800000, v117
	v_mul_f32_e32 v67, 0x42800000, v113
	v_cvt_pk_fp8_f32 v70, v72, v73 op_sel:[0,0,1]
	v_mul_f32_e32 v72, 0x42800000, v121
	v_mov_b32_e32 v71, 0
	v_cvt_pk_fp8_f32 v71, v67, v72
	v_mul_f32_e32 v73, 0x42800000, v125
	v_mul_f32_e32 v74, 0x42800000, v129
	s_lshl_b32 s24, s24, 5
	v_cvt_pk_fp8_f32 v71, v73, v74 op_sel:[0,0,1]
	v_bfe_u32 v67, v131, 3, 3
	v_or_b32_e32 v76, s24, v67
	s_movk_i32 s35, 0x90
	ds_write_b128 v66, v[134:137] offset:288
	ds_write_b128 v66, v[68:71] offset:432
	v_and_b32_e32 v162, 0x70, v132
	v_add_u32_e32 v72, s42, v76
	v_mul_lo_u32 v68, v76, s35
	s_waitcnt lgkmcnt(0)
	s_barrier
	v_add3_u32 v77, 0, v162, v68
	v_lshlrev_b32_e32 v73, 1, v72
	v_bitop3_b32 v67, s24, v211, v67 bitop3:0xc8
	s_lshl_b32 s24, s34, 7
	ds_read_b128 v[68:71], v77
	v_and_b32_e32 v73, 0xffffff00, v73
	v_or_b32_e32 v74, s24, v67
	v_add_u32_e32 v73, v74, v73
	v_cndmask_b32_e64 v74, v72, v73, s[8:9]
	v_mov_b64_e32 v[72:73], s[44:45]
	v_mad_i64_i32 v[74:75], s[34:35], s11, v74, v[72:73]
	v_lshl_add_u64 v[74:75], v[74:75], 0, v[162:163]
	v_or_b32_e32 v78, 8, v76
	s_waitcnt lgkmcnt(0)
	global_store_dwordx4 v[74:75], v[68:71], off nt
	v_add_u32_e32 v74, s42, v78
	v_lshlrev_b32_e32 v75, 1, v74
	v_bitop3_b32 v79, v76, s81, 8 bitop3:0xc8
	ds_read_b128 v[68:71], v77 offset:1152
	v_and_b32_e32 v75, 0xffffff00, v75
	v_or_b32_e32 v80, s24, v79
	v_add_u32_e32 v75, v80, v75
	v_cndmask_b32_e64 v74, v74, v75, s[8:9]
	v_mad_i64_i32 v[74:75], s[34:35], s11, v74, v[72:73]
	v_lshl_add_u64 v[74:75], v[74:75], 0, v[162:163]
	v_or_b32_e32 v80, 16, v76
	s_waitcnt lgkmcnt(0)
	global_store_dwordx4 v[74:75], v[68:71], off nt
	v_add_u32_e32 v74, s42, v80
	v_lshlrev_b32_e32 v75, 1, v74
	v_bitop3_b32 v81, v76, s82, 16 bitop3:0xc8
	ds_read_b128 v[68:71], v77 offset:2304
	v_and_b32_e32 v75, 0xffffff00, v75
	v_or_b32_e32 v82, s24, v81
	v_add_u32_e32 v75, v82, v75
	v_cndmask_b32_e64 v74, v74, v75, s[8:9]
	v_mad_i64_i32 v[74:75], s[34:35], s11, v74, v[72:73]
	v_lshl_add_u64 v[74:75], v[74:75], 0, v[162:163]
	s_waitcnt lgkmcnt(0)
	global_store_dwordx4 v[74:75], v[68:71], off nt
	v_or_b32_e32 v74, 24, v76
	v_add_u32_e32 v75, s42, v74
	s_movk_i32 s34, 0x7f
	v_lshlrev_b32_e32 v82, 1, v75
	v_bitop3_b32 v83, v76, s34, 24 bitop3:0xc8
	ds_read_b128 v[68:71], v77 offset:3456
	v_and_b32_e32 v82, 0xffffff00, v82
	v_or_b32_e32 v84, s24, v83
	v_add_u32_e32 v82, v84, v82
	v_cndmask_b32_e64 v75, v75, v82, s[8:9]
	v_mad_i64_i32 v[72:73], s[8:9], s11, v75, v[72:73]
	v_lshl_add_u64 v[72:73], v[72:73], 0, v[162:163]
	s_waitcnt lgkmcnt(0)
	global_store_dwordx4 v[72:73], v[68:71], off nt
	s_waitcnt vmcnt(7)
	v_mul_f32_e32 v2, 0x42800000, v2
	v_mul_f32_e32 v6, 0x42800000, v6
	v_mov_b32_e32 v68, v163
	v_cvt_pk_fp8_f32 v68, v2, v6
	v_mul_f32_e32 v2, 0x42800000, v14
	v_mul_f32_e32 v6, 0x42800000, v26
	v_mov_b32_e32 v69, v163
	v_cvt_pk_fp8_f32 v69, v2, v6
	v_mul_f32_e32 v2, 0x42800000, v22
	v_mul_f32_e32 v6, 0x42800000, v34
	v_mov_b32_e32 v70, v163
	v_cvt_pk_fp8_f32 v70, v2, v6
	v_mul_f32_e32 v2, 0x42800000, v46
	s_waitcnt vmcnt(6)
; #define LAS __attribute__((address_space(3)))
; #define GAS __attribute__((address_space(1)))
; __device__ __forceinline__ unsigned pk4_fp8(float a, float b, float c, float d) { int p = 0; p = __builtin_amdgcn_cvt_pk_fp8_f32(a, b, p, false); p = __builtin_amdgcn_cvt_pk_fp8_f32(c, d, p, true); return (unsigned)p; }
; __device__ __forceinline__ void tr_pack(LAS unsigned char* buf, int wave, int lane, const f32x4 (&v)[16]) {
; #pragma unroll
;     for (int j = 0; j < 4; ++j) { u32x4 o;
; #pragma unroll
;         for (int w = 0; w < 4; ++w) o[w] = pk4_fp8(64.f * v[4 * w][j], 64.f * v[4 * w + 1][j], 64.f * v[4 * w + 2][j], 64.f * v[4 * w + 3][j]);
;         *(LAS u32x4*)(buf + (4 * lane + j) * TRP + 16 * wave) = o; }
; }
; __device__ __forceinline__ void tr_flush(const TrBlk& t, const LAS unsigned char* buf, int wave, int lane) {
; #pragma unroll
;     for (int tt = 0; tt < 4; ++tt) { const int nl = 32 * wave + 8 * tt + (lane >> 3), n = 256 * t.nb + nl;
;         const u32x4 o = *(const LAS u32x4*)(buf + nl * TRP + 16 * (lane & 7));
;         const int drow = t.gu ? ((n >> 7) * 256 + (n & 127) + 128 * t.which) : n;
;         __builtin_nontemporal_store(o, (u32x4 GAS*)(t.dst + (size_t)drow * t.K + 16 * (lane & 7))); }
	v_mul_f32_e32 v6, 0x42800000, v54
	v_mov_b32_e32 v71, v163
	v_mul_f32_e32 v10, 0x42800000, v10
	v_mul_f32_e32 v18, 0x42800000, v18
	v_cvt_pk_fp8_f32 v71, v2, v6
	v_cvt_pk_fp8_f32 v68, v10, v18 op_sel:[0,0,1]
	v_mul_f32_e32 v10, 0x42800000, v30
	v_mul_f32_e32 v14, 0x42800000, v42
	v_cvt_pk_fp8_f32 v69, v10, v14 op_sel:[0,0,1]
	v_mul_f32_e32 v10, 0x42800000, v38
	v_mul_f32_e32 v14, 0x42800000, v50
	v_cvt_pk_fp8_f32 v70, v10, v14 op_sel:[0,0,1]
	s_waitcnt vmcnt(5)
	v_mul_f32_e32 v10, 0x42800000, v58
	s_waitcnt vmcnt(4)
	v_mul_f32_e32 v14, 0x42800000, v62
	v_cvt_pk_fp8_f32 v71, v10, v14 op_sel:[0,0,1]
	v_mul_f32_e32 v2, 0x42800000, v3
	v_mul_f32_e32 v3, 0x42800000, v7
	v_mul_f32_e32 v6, 0x42800000, v11
	ds_write_b128 v66, v[68:71] offset:36864
	v_mov_b32_e32 v68, v163
	v_cvt_pk_fp8_f32 v68, v2, v3
	v_mul_f32_e32 v2, 0x42800000, v15
	v_mul_f32_e32 v3, 0x42800000, v27
	v_mov_b32_e32 v69, v163
	v_cvt_pk_fp8_f32 v69, v2, v3
	v_mul_f32_e32 v2, 0x42800000, v23
	v_mul_f32_e32 v3, 0x42800000, v35
	v_mov_b32_e32 v70, v163
	v_cvt_pk_fp8_f32 v70, v2, v3
	v_mul_f32_e32 v2, 0x42800000, v47
	v_mul_f32_e32 v3, 0x42800000, v55
	v_mov_b32_e32 v71, v163
	v_mul_f32_e32 v7, 0x42800000, v19
	v_cvt_pk_fp8_f32 v71, v2, v3
	v_cvt_pk_fp8_f32 v68, v6, v7 op_sel:[0,0,1]
	v_mul_f32_e32 v6, 0x42800000, v31
	v_mul_f32_e32 v7, 0x42800000, v43
	v_cvt_pk_fp8_f32 v69, v6, v7 op_sel:[0,0,1]
	v_mul_f32_e32 v6, 0x42800000, v39
	v_mul_f32_e32 v7, 0x42800000, v51
	v_cvt_pk_fp8_f32 v70, v6, v7 op_sel:[0,0,1]
	v_mul_f32_e32 v6, 0x42800000, v59
	v_mul_f32_e32 v7, 0x42800000, v63
	v_cvt_pk_fp8_f32 v71, v6, v7 op_sel:[0,0,1]
	v_mul_f32_e32 v2, 0x42800000, v4
	v_mul_f32_e32 v3, 0x42800000, v8
	v_mul_f32_e32 v4, 0x42800000, v12
	ds_write_b128 v66, v[68:71] offset:37008
	v_mov_b32_e32 v68, v163
	v_cvt_pk_fp8_f32 v68, v2, v3
	v_mul_f32_e32 v2, 0x42800000, v16
	v_mul_f32_e32 v3, 0x42800000, v28
	v_mov_b32_e32 v69, v163
	v_cvt_pk_fp8_f32 v69, v2, v3
	v_mul_f32_e32 v2, 0x42800000, v24
	v_mul_f32_e32 v3, 0x42800000, v36
	v_mov_b32_e32 v70, v163
	v_cvt_pk_fp8_f32 v70, v2, v3
	v_mul_f32_e32 v2, 0x42800000, v48
	v_mul_f32_e32 v3, 0x42800000, v56
	v_mov_b32_e32 v71, v163
	v_mul_f32_e32 v6, 0x42800000, v20
	v_cvt_pk_fp8_f32 v71, v2, v3
	v_cvt_pk_fp8_f32 v68, v4, v6 op_sel:[0,0,1]
	v_mul_f32_e32 v4, 0x42800000, v32
	v_mul_f32_e32 v6, 0x42800000, v44
	v_cvt_pk_fp8_f32 v69, v4, v6 op_sel:[0,0,1]
	v_mul_f32_e32 v4, 0x42800000, v40
	v_mul_f32_e32 v6, 0x42800000, v52
	v_cvt_pk_fp8_f32 v70, v4, v6 op_sel:[0,0,1]
	v_mul_f32_e32 v4, 0x42800000, v60
	v_mul_f32_e32 v6, 0x42800000, v64
	v_cvt_pk_fp8_f32 v71, v4, v6 op_sel:[0,0,1]
	v_mul_f32_e32 v3, 0x42800000, v5
	v_mul_f32_e32 v4, 0x42800000, v9
	v_mov_b32_e32 v2, v163
	v_cvt_pk_fp8_f32 v2, v3, v4
	v_mul_f32_e32 v5, 0x42800000, v13
	v_mul_f32_e32 v6, 0x42800000, v21
	v_mul_f32_e32 v4, 0x42800000, v17
	v_cvt_pk_fp8_f32 v2, v5, v6 op_sel:[0,0,1]
	v_mul_f32_e32 v5, 0x42800000, v29
	v_mov_b32_e32 v3, v163
	v_cvt_pk_fp8_f32 v3, v4, v5
	v_mul_f32_e32 v6, 0x42800000, v33
	v_mul_f32_e32 v7, 0x42800000, v45
	v_mul_f32_e32 v5, 0x42800000, v25
	v_cvt_pk_fp8_f32 v3, v6, v7 op_sel:[0,0,1]
	v_mul_f32_e32 v6, 0x42800000, v37
	v_mov_b32_e32 v4, v163
	v_cvt_pk_fp8_f32 v4, v5, v6
	v_mul_f32_e32 v7, 0x42800000, v41
	v_mul_f32_e32 v8, 0x42800000, v53
	v_mul_f32_e32 v6, 0x42800000, v49
	v_cvt_pk_fp8_f32 v4, v7, v8 op_sel:[0,0,1]
	v_mul_f32_e32 v7, 0x42800000, v57
	v_mov_b32_e32 v5, v163
	v_cvt_pk_fp8_f32 v5, v6, v7
	v_mul_f32_e32 v8, 0x42800000, v61
	v_mul_f32_e32 v9, 0x42800000, v65
	ds_write_b128 v66, v[68:71] offset:37152
	v_cvt_pk_fp8_f32 v5, v8, v9 op_sel:[0,0,1]
	v_add_u32_e32 v6, s10, v76
	v_lshlrev_b32_e32 v7, 1, v6
	s_lshl_b32 s11, s18, 7
	ds_write_b128 v66, v[2:5] offset:37296
	s_waitcnt lgkmcnt(0)
	s_barrier
	ds_read_b128 v[2:5], v77 offset:36864
	v_and_b32_e32 v7, 0xffffff00, v7
	v_or_b32_e32 v8, s11, v67
	v_add_u32_e32 v7, v8, v7
	v_cndmask_b32_e64 v8, v6, v7, s[6:7]
	v_mov_b64_e32 v[6:7], s[12:13]
	v_mad_i64_i32 v[8:9], s[8:9], s19, v8, v[6:7]
	v_lshl_add_u64 v[8:9], v[8:9], 0, v[162:163]
	s_waitcnt lgkmcnt(0)
	global_store_dwordx4 v[8:9], v[2:5], off nt
	v_add_u32_e32 v8, s10, v78
	v_lshlrev_b32_e32 v9, 1, v8
	ds_read_b128 v[2:5], v77 offset:38016
	v_and_b32_e32 v9, 0xffffff00, v9
	v_or_b32_e32 v10, s11, v79
	v_add_u32_e32 v9, v10, v9
	v_cndmask_b32_e64 v8, v8, v9, s[6:7]
	v_mad_i64_i32 v[8:9], s[8:9], s19, v8, v[6:7]
	v_lshl_add_u64 v[8:9], v[8:9], 0, v[162:163]
	s_waitcnt lgkmcnt(0)
	global_store_dwordx4 v[8:9], v[2:5], off nt
	v_add_u32_e32 v8, s10, v80
	v_lshlrev_b32_e32 v9, 1, v8
	ds_read_b128 v[2:5], v77 offset:39168
	v_and_b32_e32 v9, 0xffffff00, v9
	v_or_b32_e32 v10, s11, v81
	v_add_u32_e32 v9, v10, v9
	v_cndmask_b32_e64 v8, v8, v9, s[6:7]
	v_mad_i64_i32 v[8:9], s[8:9], s19, v8, v[6:7]
	v_lshl_add_u64 v[8:9], v[8:9], 0, v[162:163]
	s_waitcnt lgkmcnt(0)
	global_store_dwordx4 v[8:9], v[2:5], off nt
	v_add_u32_e32 v8, s10, v74
	v_lshlrev_b32_e32 v9, 1, v8
	ds_read_b128 v[2:5], v77 offset:40320
	v_and_b32_e32 v9, 0xffffff00, v9
	v_or_b32_e32 v10, s11, v83
	v_add_u32_e32 v9, v10, v9
	v_cndmask_b32_e64 v8, v8, v9, s[6:7]
	v_mad_i64_i32 v[6:7], s[6:7], s19, v8, v[6:7]
	v_lshl_add_u64 v[6:7], v[6:7], 0, v[162:163]
	s_waitcnt lgkmcnt(0)
	global_store_dwordx4 v[6:7], v[2:5], off nt
	s_barrier
	s_and_saveexec_b64 s[6:7], s[4:5]
	s_cbranch_execz .LBB0_2028
	s_waitcnt vmcnt(8)
	v_add_u32_e32 v2, s3, v243
	v_cmp_eq_u32_e32 vcc, -1, v130
	s_nop 1
	v_cndmask_b32_e32 v130, v130, v2, vcc
	v_mov_b32_e32 v2, s83
	ds_write_b32 v2, v130
	s_branch .LBB0_2028
